# s3s4
# speedup vs baseline: 1.0233x; 1.0155x over previous
_Z11attn_kernelILi4EEvPKfS1_S1_S1_S1_S1_PKcPf:
	s_load_dwordx2 s[24:25], s[0:1], 0x30
	s_load_dwordx8 s[8:15], s[0:1], 0x0
	s_load_dwordx4 s[16:19], s[0:1], 0x20
	v_lshrrev_b32_e32 v63, 6, v0
	v_and_b32_e32 v104, 63, v0
	v_mad_u32_u24 v2, v63, 12, v104
	v_cmp_gt_u32_e32 vcc, 12, v104
	v_and_b32_e32 v57, 15, v0
	v_bfe_u32 v1, v0, 4, 2
	v_cndmask_b32_e32 v2, 48, v2, vcc
	v_lshlrev_b32_e32 v2, 2, v2
	v_lshlrev_b32_e32 v60, 5, v57
	v_lshlrev_b32_e32 v58, 3, v1
	v_add_u32_e32 v3, v60, v58
	v_lshrrev_b32_e32 v56, 4, v0
	v_lshlrev_b32_e32 v54, 4, v57
	v_mov_b32_e32 v59, 0
	s_movk_i32 s4, 0xe0
	v_cmp_gt_u32_e64 s[4:5], s4, v0
	s_lshl_b32 s26, s2, 8
	s_lshl_b32 s27, s2, 9
	s_mul_i32 s28, s2, 14
	v_lshlrev_b32_e32 v5, 2, v57
	v_lshlrev_b32_e32 v147, 6, v57
	s_waitcnt lgkmcnt(0)
	s_add_u32 s20, s24, s26
	s_addc_u32 s21, s25, 0
	s_add_u32 s20, s20, 0x164000
	s_addc_u32 s21, s21, 0
	s_add_u32 s26, s24, s27
	s_addc_u32 s27, s25, 0
	s_add_u32 s26, s26, 0x80000
	s_addc_u32 s27, s27, 0
	global_load_dword v61, v2, s[20:21]
	global_load_dwordx2 v[64:65], v3, s[26:27]
	s_add_u32 s22, s24, 0x160000
	s_addc_u32 s23, s25, 0
	v_cndmask_b32_e64 v62, 13, v56, s[4:5]
	v_add_u32_e32 v3, s28, v62
	v_mad_u32_u24 v144, v3, 36, v5
	v_mad_u32_u24 v146, v3, 12, v5
	v_add_u32_e32 v145, -36, v146
	v_add_u32_e32 v146, -48, v146
	v_lshl_or_b32 v147, v63, 10, v147
	v_lshl_or_b32 v147, v1, 4, v147
	v_or_b32_e32 v148, 0x1000, v147
	v_lshlrev_b32_e32 v149, 4, v104
	v_lshlrev_b32_e32 v150, 9, v3
	v_add_u32_e32 v150, v150, v54
	s_waitcnt vmcnt(1)
	v_readlane_b32 s3, v61, 12
	s_bitcmp0_b32 s3, 1
	s_cselect_b64 s[20:21], -1, 0
	s_cbranch_scc1 .LBB1_16
	v_and_b32_e32 v3, 12, v57
	v_lshlrev_b32_e32 v19, 2, v1
	ds_bpermute_b32 v81, v3, v61
	ds_bpermute_b32 v82, v3, v61 offset:16
	ds_bpermute_b32 v83, v3, v61 offset:32
	ds_bpermute_b32 v84, v19, v61
	ds_bpermute_b32 v85, v19, v61 offset:16
	ds_bpermute_b32 v86, v19, v61 offset:32
	v_and_b32_e32 v87, 3, v57
	v_lshlrev_b32_e32 v87, 4, v87
	v_lshl_or_b32 v87, v1, 6, v87
	v_lshlrev_b32_e32 v88, 3, v57
	s_add_u32 s26, s24, 0x100000
	s_addc_u32 s27, s25, 0
	s_add_u32 s28, s24, 0x140000
	s_addc_u32 s29, s25, 0
	s_waitcnt lgkmcnt(3)
	v_lshl_add_u32 v72, v81, 9, v87
	v_lshl_add_u32 v73, v82, 9, v87
	v_lshl_add_u32 v74, v83, 9, v87
	global_load_dwordx4 v[50:53], v72, s[24:25]
	global_load_dwordx4 v[46:49], v72, s[24:25] offset:256
	global_load_dwordx4 v[14:17], v73, s[24:25]
	global_load_dwordx4 v[10:13], v73, s[24:25] offset:256
	global_load_dwordx4 v[6:9], v74, s[24:25]
	global_load_dwordx4 v[2:5], v74, s[24:25] offset:256
	s_waitcnt lgkmcnt(0)
	v_lshl_add_u32 v75, v84, 8, v54
	v_lshl_add_u32 v78, v84, 7, v88
	v_lshl_add_u32 v76, v85, 8, v54
	v_lshl_add_u32 v79, v85, 7, v88
	v_lshl_add_u32 v77, v86, 8, v54
	v_lshl_add_u32 v80, v86, 7, v88
	global_load_dwordx4 v[30:33], v75, s[26:27]
	global_load_dwordx2 v[70:71], v78, s[28:29]
	global_load_dwordx4 v[26:29], v76, s[26:27]
	global_load_dwordx2 v[66:67], v79, s[28:29]
	global_load_dwordx4 v[18:21], v77, s[26:27]
	global_load_dwordx2 v[68:69], v80, s[28:29]
	s_mov_b32 exec_lo, 0x1ff01ff
	s_mov_b32 exec_hi, 0x1ff01ff
	global_load_dword v120, v144, s[10:11]
	s_mov_b32 exec_lo, 0xe000e00
	s_mov_b32 exec_hi, 0xe000e00
	global_load_dword v120, v145, s[12:13]
	s_mov_b32 exec_lo, 0x70007000
	s_mov_b32 exec_hi, 0x70007000
	global_load_dword v120, v146, s[14:15]
	s_mov_b64 exec, -1
	global_load_dwordx4 v[124:127], v147, s[22:23]
	global_load_dwordx4 v[128:131], v148, s[22:23]
	s_mov_b32 exec_hi, 0
	global_load_dwordx4 v[132:135], v149, s[16:17]
	s_mov_b32 exec_hi, -1
	s_mov_b32 exec_lo, 0
	global_load_dwordx4 v[132:135], v149, s[18:19] offset:-512
	s_mov_b32 exec_lo, -1
	global_load_dwordx4 v[136:139], v150, s[8:9]
	global_load_dwordx4 v[140:143], v150, s[8:9] offset:256
	s_movk_i32 s6, 0x140
	v_cmp_gt_u32_e32 vcc, s6, v0
	v_lshlrev_b32_e32 v22, 2, v0
	v_mov_b32_e32 v23, 0
	s_and_saveexec_b64 s[6:7], vcc
	ds_write_b32 v22, v23 offset:14336
	s_or_b64 exec, exec, s[6:7]
	v_cmp_gt_u32_e32 vcc, 64, v0
	s_and_saveexec_b64 s[6:7], vcc
	ds_write_b32 v22, v23 offset:15360
	s_or_b64 exec, exec, s[6:7]
	v_bfe_u32 v22, s3, v57, 1
	v_cmp_eq_u32_e32 vcc, 0, v22
	v_mov_b32_e32 v45, 0xc9c35000
	s_mov_b32 s30, 0x3db8aa3b
	s_mov_b32 s31, 0x3db8aa3b
	v_cndmask_b32_e64 v55, 1.0, 0, vcc
	v_mov_b32_e32 v121, 0x3fb8aa3b
	s_bitcmp0_b32 s3, 0
	s_cselect_b64 vcc, -1, 0
	v_cndmask_b32_e32 v34, 0, v45, vcc
	s_bitcmp0_b32 s3, 2
	s_cselect_b64 vcc, -1, 0
	v_cndmask_b32_e32 v36, 0, v45, vcc
	s_bitcmp0_b32 s3, 3
	s_cselect_b64 vcc, -1, 0
	v_cndmask_b32_e32 v37, 0, v45, vcc
	s_bitcmp0_b32 s3, 4
	s_cselect_b64 vcc, -1, 0
	v_cndmask_b32_e32 v22, 0, v45, vcc
	s_bitcmp0_b32 s3, 5
	s_cselect_b64 vcc, -1, 0
	v_cndmask_b32_e32 v23, 0, v45, vcc
	s_bitcmp0_b32 s3, 6
	s_cselect_b64 vcc, -1, 0
	v_cndmask_b32_e32 v24, 0, v45, vcc
	s_bitcmp0_b32 s3, 7
	s_cselect_b64 vcc, -1, 0
	v_cndmask_b32_e32 v25, 0, v45, vcc
	s_bitcmp0_b32 s3, 8
	s_cselect_b64 vcc, -1, 0
	v_cndmask_b32_e32 v38, 0, v45, vcc
	s_bitcmp0_b32 s3, 9
	s_cselect_b64 vcc, -1, 0
	v_cndmask_b32_e32 v39, 0, v45, vcc
	s_bitcmp0_b32 s3, 10
	s_cselect_b64 vcc, -1, 0
	v_cndmask_b32_e32 v40, 0, v45, vcc
	s_bitcmp0_b32 s3, 11
	s_cselect_b64 vcc, -1, 0
	v_cndmask_b32_e32 v41, 0, v45, vcc
	s_bitcmp0_b32 s3, 12
	s_cselect_b64 vcc, -1, 0
	v_cndmask_b32_e32 v42, 0, v45, vcc
	s_bitcmp0_b32 s3, 13
	s_cselect_b64 vcc, -1, 0
	v_cndmask_b32_e32 v43, 0, v45, vcc
	v_mov_b32_e32 v35, 0
	v_mov_b32_e32 v44, v45
	v_mov_b32_e32 v75, 0
	v_mov_b32_e32 v79, 0
	v_mov_b32_e32 v83, 0
	s_waitcnt vmcnt(20)
	v_mfma_f32_16x16x32_fp8_fp8 v[160:163], v[50:51], v[64:65], v[34:37]
	v_mfma_f32_16x16x32_fp8_fp8 v[164:167], v[52:53], v[64:65], v[22:25]
	s_waitcnt vmcnt(19)
	v_mfma_f32_16x16x32_fp8_fp8 v[168:171], v[46:47], v[64:65], v[38:41]
	v_mfma_f32_16x16x32_fp8_fp8 v[172:175], v[48:49], v[64:65], v[42:45]
	s_nop 3
	v_max3_f32 v86, v160, v161, v162
	v_max3_f32 v87, v163, v164, v165
	v_max3_f32 v88, v166, v167, v168
	v_max3_f32 v89, v169, v170, v171
	v_max3_f32 v86, v86, v172, v173
	v_max3_f32 v87, v87, v88, v89
	v_max_f32_e32 v96, v86, v87
	v_mul_f32_e32 v98, 0xbdb8aa3b, v96
	v_pk_fma_f32 v[208:209], v[160:161], s[30:31], v[98:99] op_sel_hi:[1,1,0]
	v_pk_fma_f32 v[210:211], v[162:163], s[30:31], v[98:99] op_sel_hi:[1,1,0]
	v_pk_fma_f32 v[212:213], v[164:165], s[30:31], v[98:99] op_sel_hi:[1,1,0]
	v_pk_fma_f32 v[214:215], v[166:167], s[30:31], v[98:99] op_sel_hi:[1,1,0]
	v_pk_fma_f32 v[216:217], v[168:169], s[30:31], v[98:99] op_sel_hi:[1,1,0]
	v_pk_fma_f32 v[218:219], v[170:171], s[30:31], v[98:99] op_sel_hi:[1,1,0]
	v_pk_fma_f32 v[220:221], v[172:173], s[30:31], v[98:99] op_sel_hi:[1,1,0]
	v_exp_f32_e32 v208, v208
	v_exp_f32_e32 v209, v209
	v_exp_f32_e32 v210, v210
	v_exp_f32_e32 v211, v211
	v_exp_f32_e32 v212, v212
	v_exp_f32_e32 v213, v213
	v_exp_f32_e32 v214, v214
	v_exp_f32_e32 v215, v215
	v_exp_f32_e32 v216, v216
	v_exp_f32_e32 v217, v217
	v_exp_f32_e32 v218, v218
	v_exp_f32_e32 v219, v219
	v_exp_f32_e32 v220, v220
	v_exp_f32_e32 v221, v221
	s_waitcnt vmcnt(18)
	v_mfma_f32_16x16x32_fp8_fp8 v[176:179], v[14:15], v[64:65], v[34:37]
	v_mfma_f32_16x16x32_fp8_fp8 v[180:183], v[16:17], v[64:65], v[22:25]
	s_waitcnt vmcnt(17)
	v_mfma_f32_16x16x32_fp8_fp8 v[184:187], v[10:11], v[64:65], v[38:41]
	v_mfma_f32_16x16x32_fp8_fp8 v[188:191], v[12:13], v[64:65], v[42:45]
	v_pk_add_f32 v[86:87], v[208:209], v[210:211]
	v_pk_add_f32 v[88:89], v[212:213], v[214:215]
	v_pk_add_f32 v[90:91], v[216:217], v[218:219]
	v_pk_mul_f32 v[92:93], v[208:209], v[160:161]
	v_pk_mul_f32 v[94:95], v[210:211], v[162:163]
	v_pk_add_f32 v[86:87], v[86:87], v[220:221]
	v_pk_add_f32 v[88:89], v[88:89], v[90:91]
	v_pk_fma_f32 v[92:93], v[212:213], v[164:165], v[92:93]
	v_pk_fma_f32 v[94:95], v[214:215], v[166:167], v[94:95]
	v_pk_add_f32 v[86:87], v[86:87], v[88:89]
	v_pk_fma_f32 v[92:93], v[216:217], v[168:169], v[92:93]
	v_pk_fma_f32 v[94:95], v[218:219], v[170:171], v[94:95]
	v_add_f32_e32 v86, v86, v87
	v_pk_fma_f32 v[92:93], v[220:221], v[172:173], v[92:93]
	v_rcp_f32_e32 v87, v86
	v_pk_add_f32 v[92:93], v[92:93], v[94:95]
	v_mul_f32_e32 v87, v55, v87
	v_add_f32_e32 v92, v92, v93
	v_mul_f32_e32 v107, v86, v87
	v_mul_f32_e32 v92, v92, v87
	v_mul_f32_e32 v100, 0x43800000, v87
	v_mul_f32_e32 v103, 0x3d800000, v92
	v_max3_f32 v86, v176, v177, v178
	v_max3_f32 v87, v179, v180, v181
	v_max3_f32 v88, v182, v183, v184
	v_max3_f32 v89, v185, v186, v187
	v_max3_f32 v86, v86, v188, v189
	v_max3_f32 v87, v87, v88, v89
	v_max_f32_e32 v96, v86, v87
	v_mul_f32_e32 v98, 0xbdb8aa3b, v96
	v_pk_fma_f32 v[222:223], v[176:177], s[30:31], v[98:99] op_sel_hi:[1,1,0]
	v_pk_fma_f32 v[224:225], v[178:179], s[30:31], v[98:99] op_sel_hi:[1,1,0]
	v_pk_fma_f32 v[226:227], v[180:181], s[30:31], v[98:99] op_sel_hi:[1,1,0]
	v_pk_fma_f32 v[228:229], v[182:183], s[30:31], v[98:99] op_sel_hi:[1,1,0]
	v_pk_fma_f32 v[230:231], v[184:185], s[30:31], v[98:99] op_sel_hi:[1,1,0]
	v_pk_fma_f32 v[232:233], v[186:187], s[30:31], v[98:99] op_sel_hi:[1,1,0]
	v_pk_fma_f32 v[234:235], v[188:189], s[30:31], v[98:99] op_sel_hi:[1,1,0]
	v_exp_f32_e32 v222, v222
	v_exp_f32_e32 v223, v223
	v_exp_f32_e32 v224, v224
	v_exp_f32_e32 v225, v225
	v_exp_f32_e32 v226, v226
	v_exp_f32_e32 v227, v227
	v_exp_f32_e32 v228, v228
	v_exp_f32_e32 v229, v229
	v_exp_f32_e32 v230, v230
	v_exp_f32_e32 v231, v231
	v_exp_f32_e32 v232, v232
	v_exp_f32_e32 v233, v233
	v_exp_f32_e32 v234, v234
	v_exp_f32_e32 v235, v235
	s_waitcnt vmcnt(16)
	v_mfma_f32_16x16x32_fp8_fp8 v[192:195], v[6:7], v[64:65], v[34:37]
	v_mfma_f32_16x16x32_fp8_fp8 v[196:199], v[8:9], v[64:65], v[22:25]
	s_waitcnt vmcnt(15)
	v_mfma_f32_16x16x32_fp8_fp8 v[200:203], v[2:3], v[64:65], v[38:41]
	v_mfma_f32_16x16x32_fp8_fp8 v[204:207], v[4:5], v[64:65], v[42:45]
	v_pk_add_f32 v[86:87], v[222:223], v[224:225]
	v_pk_add_f32 v[88:89], v[226:227], v[228:229]
	v_pk_add_f32 v[90:91], v[230:231], v[232:233]
	v_pk_mul_f32 v[92:93], v[222:223], v[176:177]
	v_pk_mul_f32 v[94:95], v[224:225], v[178:179]
	v_pk_add_f32 v[86:87], v[86:87], v[234:235]
	v_pk_add_f32 v[88:89], v[88:89], v[90:91]
	v_pk_fma_f32 v[92:93], v[226:227], v[180:181], v[92:93]
	v_pk_fma_f32 v[94:95], v[228:229], v[182:183], v[94:95]
	v_pk_add_f32 v[86:87], v[86:87], v[88:89]
	v_pk_fma_f32 v[92:93], v[230:231], v[184:185], v[92:93]
	v_pk_fma_f32 v[94:95], v[232:233], v[186:187], v[94:95]
	v_add_f32_e32 v86, v86, v87
	v_pk_fma_f32 v[92:93], v[234:235], v[188:189], v[92:93]
	v_rcp_f32_e32 v87, v86
	v_pk_add_f32 v[92:93], v[92:93], v[94:95]
	v_mul_f32_e32 v87, v55, v87
	v_add_f32_e32 v92, v92, v93
	v_mul_f32_e32 v108, v86, v87
	v_mul_f32_e32 v92, v92, v87
	v_mul_f32_e32 v101, 0x43800000, v87
	v_mul_f32_e32 v105, 0x3d800000, v92
	v_max3_f32 v86, v192, v193, v194
	v_max3_f32 v87, v195, v196, v197
	v_max3_f32 v88, v198, v199, v200
	v_max3_f32 v89, v201, v202, v203
	v_max3_f32 v86, v86, v204, v205
	v_max3_f32 v87, v87, v88, v89
	v_max_f32_e32 v96, v86, v87
	v_mul_f32_e32 v98, 0xbdb8aa3b, v96
	v_pk_fma_f32 v[236:237], v[192:193], s[30:31], v[98:99] op_sel_hi:[1,1,0]
	v_pk_fma_f32 v[238:239], v[194:195], s[30:31], v[98:99] op_sel_hi:[1,1,0]
	v_pk_fma_f32 v[240:241], v[196:197], s[30:31], v[98:99] op_sel_hi:[1,1,0]
	v_pk_fma_f32 v[242:243], v[198:199], s[30:31], v[98:99] op_sel_hi:[1,1,0]
	v_pk_fma_f32 v[244:245], v[200:201], s[30:31], v[98:99] op_sel_hi:[1,1,0]
	v_pk_fma_f32 v[246:247], v[202:203], s[30:31], v[98:99] op_sel_hi:[1,1,0]
	v_pk_fma_f32 v[248:249], v[204:205], s[30:31], v[98:99] op_sel_hi:[1,1,0]
	v_exp_f32_e32 v236, v236
	v_exp_f32_e32 v237, v237
	v_exp_f32_e32 v238, v238
	v_exp_f32_e32 v239, v239
	v_exp_f32_e32 v240, v240
	v_exp_f32_e32 v241, v241
	v_exp_f32_e32 v242, v242
	v_exp_f32_e32 v243, v243
	v_exp_f32_e32 v244, v244
	v_exp_f32_e32 v245, v245
	v_exp_f32_e32 v246, v246
	v_exp_f32_e32 v247, v247
	v_exp_f32_e32 v248, v248
	v_exp_f32_e32 v249, v249
	v_pk_add_f32 v[86:87], v[236:237], v[238:239]
	v_pk_add_f32 v[88:89], v[240:241], v[242:243]
	v_pk_add_f32 v[90:91], v[244:245], v[246:247]
	v_pk_mul_f32 v[92:93], v[236:237], v[192:193]
	v_pk_mul_f32 v[94:95], v[238:239], v[194:195]
	v_pk_add_f32 v[86:87], v[86:87], v[248:249]
	v_pk_add_f32 v[88:89], v[88:89], v[90:91]
	v_pk_fma_f32 v[92:93], v[240:241], v[196:197], v[92:93]
	v_pk_fma_f32 v[94:95], v[242:243], v[198:199], v[94:95]
	v_pk_add_f32 v[86:87], v[86:87], v[88:89]
	v_pk_fma_f32 v[92:93], v[244:245], v[200:201], v[92:93]
	v_pk_fma_f32 v[94:95], v[246:247], v[202:203], v[94:95]
	v_add_f32_e32 v86, v86, v87
	v_pk_fma_f32 v[92:93], v[248:249], v[204:205], v[92:93]
	v_rcp_f32_e32 v87, v86
	v_pk_add_f32 v[92:93], v[92:93], v[94:95]
	v_mul_f32_e32 v87, v55, v87
	v_add_f32_e32 v92, v92, v93
	v_mul_f32_e32 v109, v86, v87
	v_mul_f32_e32 v92, v92, v87
	v_mul_f32_e32 v102, 0x43800000, v87
	v_mul_f32_e32 v106, 0x3d800000, v92
	v_max3_f32 v122, v103, v105, v106
	v_cmp_gt_u32_e64 s[6:7], 16, v104
	v_mov_b32_e32 v123, v122
	s_nop 1
	v_permlane16_swap_b32_e32 v122, v123
	v_max_f32_e32 v122, v122, v123
	v_mov_b32_e32 v123, v122
	s_nop 1
	v_permlane32_swap_b32_e32 v122, v123
	v_max_f32_e32 v36, v122, v123
	v_mul_f32_e32 v123, 0x3fb8aa3b, v36
	v_fma_f32 v111, v103, v121, -v123
	v_exp_f32_e32 v111, v111
	s_nop 0
	v_mul_f32_e32 v112, v111, v100
	v_mul_f32_e32 v110, v111, v107
	v_mov_b32_e32 v114, v111
	v_pk_mul_f32 v[208:209], v[208:209], v[112:113] op_sel_hi:[1,0]
	v_pk_mul_f32 v[210:211], v[210:211], v[112:113] op_sel_hi:[1,0]
	v_pk_mul_f32 v[212:213], v[212:213], v[112:113] op_sel_hi:[1,0]
	v_pk_mul_f32 v[214:215], v[214:215], v[112:113] op_sel_hi:[1,0]
	v_pk_mul_f32 v[216:217], v[216:217], v[112:113] op_sel_hi:[1,0]
	v_pk_mul_f32 v[218:219], v[218:219], v[112:113] op_sel_hi:[1,0]
	v_pk_mul_f32 v[220:221], v[220:221], v[112:113] op_sel_hi:[1,0]
	s_waitcnt vmcnt(13)
	v_mov_b32_e32 v115, v110
	v_fma_mix_f32 v116, v110, v70, 0 op_sel_hi:[0,1,0]
	v_fma_mix_f32 v117, v110, v70, 0 op_sel:[0,1,0] op_sel_hi:[0,1,0]
	v_fma_mix_f32 v118, v110, v71, 0 op_sel_hi:[0,1,0]
	v_cvt_pk_fp8_f32 v72, v208, v209
	v_cvt_pk_fp8_f32 v73, v212, v213
	v_cvt_pk_fp8_f32 v74, v216, v217
	v_cvt_pk_fp8_f32 v75, v220, v221
	v_cvt_pk_fp8_f32 v72, v210, v211 op_sel:[0,0,1]
	v_cvt_pk_fp8_f32 v73, v214, v215 op_sel:[0,0,1]
	v_cvt_pk_fp8_f32 v74, v218, v219 op_sel:[0,0,1]
	s_nop 1
	v_mfma_f32_16x16x32_fp8_fp8 v[152:155], v[72:73], v[30:31], 0
	v_mfma_f32_16x16x32_fp8_fp8 v[152:155], v[74:75], v[32:33], v[152:155]
	v_fma_f32 v111, v105, v121, -v123
	v_exp_f32_e32 v111, v111
	s_nop 0
	v_mul_f32_e32 v112, v111, v101
	v_mul_f32_e32 v110, v111, v108
	v_add_f32_e32 v114, v114, v111
	v_pk_mul_f32 v[222:223], v[222:223], v[112:113] op_sel_hi:[1,0]
	v_pk_mul_f32 v[224:225], v[224:225], v[112:113] op_sel_hi:[1,0]
	v_pk_mul_f32 v[226:227], v[226:227], v[112:113] op_sel_hi:[1,0]
	v_pk_mul_f32 v[228:229], v[228:229], v[112:113] op_sel_hi:[1,0]
	v_pk_mul_f32 v[230:231], v[230:231], v[112:113] op_sel_hi:[1,0]
	v_pk_mul_f32 v[232:233], v[232:233], v[112:113] op_sel_hi:[1,0]
	v_pk_mul_f32 v[234:235], v[234:235], v[112:113] op_sel_hi:[1,0]
	s_waitcnt vmcnt(11)
	v_add_f32_e32 v115, v115, v110
	v_fma_mix_f32 v116, v110, v66, v116 op_sel_hi:[0,1,0]
	v_fma_mix_f32 v117, v110, v66, v117 op_sel:[0,1,0] op_sel_hi:[0,1,0]
	v_fma_mix_f32 v118, v110, v67, v118 op_sel_hi:[0,1,0]
	v_cvt_pk_fp8_f32 v76, v222, v223
	v_cvt_pk_fp8_f32 v77, v226, v227
	v_cvt_pk_fp8_f32 v78, v230, v231
	v_cvt_pk_fp8_f32 v79, v234, v235
	v_cvt_pk_fp8_f32 v76, v224, v225 op_sel:[0,0,1]
	v_cvt_pk_fp8_f32 v77, v228, v229 op_sel:[0,0,1]
	v_cvt_pk_fp8_f32 v78, v232, v233 op_sel:[0,0,1]
	s_nop 1
	v_mfma_f32_16x16x32_fp8_fp8 v[152:155], v[76:77], v[26:27], v[152:155]
	v_mfma_f32_16x16x32_fp8_fp8 v[152:155], v[78:79], v[28:29], v[152:155]
	v_fma_f32 v111, v106, v121, -v123
	v_exp_f32_e32 v111, v111
	s_nop 0
	v_mul_f32_e32 v112, v111, v102
	v_mul_f32_e32 v110, v111, v109
	v_add_f32_e32 v114, v114, v111
	v_pk_mul_f32 v[236:237], v[236:237], v[112:113] op_sel_hi:[1,0]
	v_pk_mul_f32 v[238:239], v[238:239], v[112:113] op_sel_hi:[1,0]
	v_pk_mul_f32 v[240:241], v[240:241], v[112:113] op_sel_hi:[1,0]
	v_pk_mul_f32 v[242:243], v[242:243], v[112:113] op_sel_hi:[1,0]
	v_pk_mul_f32 v[244:245], v[244:245], v[112:113] op_sel_hi:[1,0]
	v_pk_mul_f32 v[246:247], v[246:247], v[112:113] op_sel_hi:[1,0]
	v_pk_mul_f32 v[248:249], v[248:249], v[112:113] op_sel_hi:[1,0]
	s_waitcnt vmcnt(9)
	v_add_f32_e32 v115, v115, v110
	v_fma_mix_f32 v116, v110, v68, v116 op_sel_hi:[0,1,0]
	v_fma_mix_f32 v117, v110, v68, v117 op_sel:[0,1,0] op_sel_hi:[0,1,0]
	v_fma_mix_f32 v118, v110, v69, v118 op_sel_hi:[0,1,0]
	v_cvt_pk_fp8_f32 v80, v236, v237
	v_cvt_pk_fp8_f32 v81, v240, v241
	v_cvt_pk_fp8_f32 v82, v244, v245
	v_cvt_pk_fp8_f32 v83, v248, v249
	v_cvt_pk_fp8_f32 v80, v238, v239 op_sel:[0,0,1]
	v_cvt_pk_fp8_f32 v81, v242, v243 op_sel:[0,0,1]
	v_cvt_pk_fp8_f32 v82, v246, v247 op_sel:[0,0,1]
	s_nop 1
	v_mfma_f32_16x16x32_fp8_fp8 v[152:155], v[80:81], v[18:19], v[152:155]
	v_mfma_f32_16x16x32_fp8_fp8 v[152:155], v[82:83], v[20:21], v[152:155]
	v_mov_b32_e32 v86, v114
	v_mov_b32_e32 v87, v115
	v_mov_b32_e32 v88, v116
	v_mov_b32_e32 v89, v117
	v_mov_b32_e32 v90, v118
	v_permlane16_swap_b32_e32 v114, v86
	v_permlane16_swap_b32_e32 v115, v87
	v_permlane16_swap_b32_e32 v116, v88
	v_permlane16_swap_b32_e32 v117, v89
	v_permlane16_swap_b32_e32 v118, v90
	v_add_f32_e32 v114, v114, v86
	v_add_f32_e32 v115, v115, v87
	v_add_f32_e32 v116, v116, v88
	v_add_f32_e32 v117, v117, v89
	v_add_f32_e32 v118, v118, v90
	v_mov_b32_e32 v86, v114
	v_mov_b32_e32 v87, v115
	v_mov_b32_e32 v88, v116
	v_mov_b32_e32 v89, v117
	v_mov_b32_e32 v90, v118
	v_permlane32_swap_b32_e32 v114, v86
	v_permlane32_swap_b32_e32 v115, v87
	v_permlane32_swap_b32_e32 v116, v88
	v_permlane32_swap_b32_e32 v117, v89
	v_permlane32_swap_b32_e32 v118, v90
	v_mul_u32_u24_e32 v91, 0x140, v1
	s_movk_i32 s26, 0x500
	v_mad_u32_u24 v91, v63, s26, v91
	v_lshl_or_b32 v91, v57, 2, v91
	v_add_u32_e32 v91, 0x1c00, v91
	v_add_f32_e32 v37, v114, v86
	v_add_f32_e32 v20, v115, v87
	v_add_f32_e32 v18, v116, v88
	v_add_f32_e32 v19, v117, v89
	v_add_f32_e32 v21, v118, v90
	ds_write2_b32 v91, v152, v153 offset0:0 offset1:20
	ds_write2_b32 v91, v154, v155 offset0:40 offset1:60
	s_branch .LBB1_30

	.amdhsa_kernel _Z11attn_kernelILi4EEvPKfS1_S1_S1_S1_S1_PKcPf
		.amdhsa_group_segment_fixed_size 16640
		.amdhsa_private_segment_fixed_size 0
		.amdhsa_kernarg_size 64
		.amdhsa_user_sgpr_count 2
		.amdhsa_user_sgpr_dispatch_ptr 0
		.amdhsa_user_sgpr_queue_ptr 0
		.amdhsa_user_sgpr_kernarg_segment_ptr 1
		.amdhsa_user_sgpr_dispatch_id 0
		.amdhsa_user_sgpr_kernarg_preload_length 0
		.amdhsa_user_sgpr_kernarg_preload_offset 0
		.amdhsa_user_sgpr_private_segment_size 0
		.amdhsa_uses_dynamic_stack 0
		.amdhsa_enable_private_segment 0
		.amdhsa_system_sgpr_workgroup_id_x 1
		.amdhsa_system_sgpr_workgroup_id_y 0
		.amdhsa_system_sgpr_workgroup_id_z 0
		.amdhsa_system_sgpr_workgroup_info 0
		.amdhsa_system_vgpr_workitem_id 0
		.amdhsa_next_free_vgpr 250
		.amdhsa_next_free_sgpr 32
		.amdhsa_accum_offset 252
		.amdhsa_reserve_vcc 1
		.amdhsa_float_round_mode_32 0
		.amdhsa_float_round_mode_16_64 0
		.amdhsa_float_denorm_mode_32 3
		.amdhsa_float_denorm_mode_16_64 3
		.amdhsa_dx10_clamp 1
		.amdhsa_ieee_mode 1
		.amdhsa_fp16_overflow 0
		.amdhsa_tg_split 0
		.amdhsa_exception_fp_ieee_invalid_op 0
		.amdhsa_exception_fp_denorm_src 0
		.amdhsa_exception_fp_ieee_div_zero 0
		.amdhsa_exception_fp_ieee_overflow 0
		.amdhsa_exception_fp_ieee_underflow 0
		.amdhsa_exception_fp_ieee_inexact 0
		.amdhsa_exception_int_div_zero 0
	.end_amdhsa_kernel

amdhsa.kernels:
  - .agpr_count:     12
    .args:
      - .actual_access:  read_only
        .address_space:  global
        .offset:         0
        .size:           8
        .value_kind:     global_buffer
      - .actual_access:  read_only
        .address_space:  global
        .offset:         8
        .size:           8
        .value_kind:     global_buffer
      - .actual_access:  read_only
        .address_space:  global
        .offset:         16
        .size:           8
        .value_kind:     global_buffer
      - .actual_access:  read_only
        .address_space:  global
        .offset:         24
        .size:           8
        .value_kind:     global_buffer
      - .actual_access:  read_only
        .address_space:  global
        .offset:         32
        .size:           8
        .value_kind:     global_buffer
      - .actual_access:  read_only
        .address_space:  global
        .offset:         40
        .size:           8
        .value_kind:     global_buffer
      - .actual_access:  read_only
        .address_space:  global
        .offset:         48
        .size:           8
        .value_kind:     global_buffer
      - .actual_access:  read_only
        .address_space:  global
        .offset:         56
        .size:           8
        .value_kind:     global_buffer
      - .actual_access:  read_only
        .address_space:  global
        .offset:         64
        .size:           8
        .value_kind:     global_buffer
      - .actual_access:  read_only
        .address_space:  global
        .offset:         72
        .size:           8
        .value_kind:     global_buffer
      - .actual_access:  write_only
        .address_space:  global
        .offset:         80
        .size:           8
        .value_kind:     global_buffer
    .group_segment_fixed_size: 13056
    .kernarg_segment_align: 8
    .kernarg_segment_size: 88
    .language:       OpenCL C
    .language_version:
      - 2
      - 0
    .max_flat_workgroup_size: 128
    .name:           _Z11prep_kernelPKfS0_PKiS2_S0_S0_S0_S0_S0_S0_Pc
    .private_segment_fixed_size: 0
    .sgpr_count:     38
    .sgpr_spill_count: 0
    .symbol:         _Z11prep_kernelPKfS0_PKiS2_S0_S0_S0_S0_S0_S0_Pc.kd
    .uniform_work_group_size: 1
    .uses_dynamic_stack: false
    .vgpr_count:     136
    .vgpr_spill_count: 0
    .wavefront_size: 64
  - .agpr_count:     0
    .args:
      - .actual_access:  read_only
        .address_space:  global
        .offset:         0
        .size:           8
        .value_kind:     global_buffer
      - .actual_access:  read_only
        .address_space:  global
        .offset:         8
        .size:           8
        .value_kind:     global_buffer
      - .actual_access:  read_only
        .address_space:  global
        .offset:         16
        .size:           8
        .value_kind:     global_buffer
      - .actual_access:  read_only
        .address_space:  global
        .offset:         24
        .size:           8
        .value_kind:     global_buffer
      - .actual_access:  read_only
        .address_space:  global
        .offset:         32
        .size:           8
        .value_kind:     global_buffer
      - .actual_access:  read_only
        .address_space:  global
        .offset:         40
        .size:           8
        .value_kind:     global_buffer
      - .actual_access:  read_only
        .address_space:  global
        .offset:         48
        .size:           8
        .value_kind:     global_buffer
      - .actual_access:  write_only
        .address_space:  global
        .offset:         56
        .size:           8
        .value_kind:     global_buffer
    .group_segment_fixed_size: 16640
    .kernarg_segment_align: 8
    .kernarg_segment_size: 64
    .language:       OpenCL C
    .language_version:
      - 2
      - 0
    .max_flat_workgroup_size: 256
    .name:           _Z11attn_kernelILi4EEvPKfS1_S1_S1_S1_S1_PKcPf
    .private_segment_fixed_size: 0
    .sgpr_count:     38
    .sgpr_spill_count: 0
    .symbol:         _Z11attn_kernelILi4EEvPKfS1_S1_S1_S1_S1_PKcPf.kd
    .uniform_work_group_size: 1
    .uses_dynamic_stack: false
    .vgpr_count:     250
    .vgpr_spill_count: 0
    .wavefront_size: 64
